# GEMM phases: redundant accumulator clear skipped in 24 of 25 phases
# speedup vs baseline: 1.0063x; 1.0024x over previous
;     ...
;         for (int t = 0; t < nt; t += 2) {
;     ...
; #pragma unroll
;         for (int a = 0; a < 2; ++a)
; #pragma unroll
;             for (int b = 0; b < 2; ++b)
; #pragma unroll
;                 for (int m = 0; m < 4; ++m)
; #pragma unroll
;                     for (int n = 0; n < 2; ++n) acc[a][b][m][n] = (f32x4){0.f, 0.f, 0.f, 0.f};
.LBB0_301:
	v_mov_b32_e32 v129, 0
	s_andn2_b64 vcc, exec, s[14:15]
	s_cbranch_vccz .Lzt_1
	v_mov_b32_e32 v128, 0
	v_mov_b32_e32 v127, 0
	v_mov_b32_e32 v126, 0
	v_mov_b32_e32 v147, 0
	v_mov_b32_e32 v146, 0
	v_mov_b32_e32 v149, 0
	v_mov_b32_e32 v148, 0
	v_mov_b32_e32 v111, 0
	v_mov_b32_e32 v110, 0
	v_mov_b32_e32 v113, 0
	v_mov_b32_e32 v112, 0
	v_mov_b32_e32 v117, 0
	v_mov_b32_e32 v116, 0
	v_mov_b32_e32 v115, 0
	v_mov_b32_e32 v114, 0
	v_mov_b32_e32 v95, 0
	v_mov_b32_e32 v94, 0
	v_mov_b32_e32 v97, 0
	v_mov_b32_e32 v96, 0
	v_mov_b32_e32 v101, 0
	v_mov_b32_e32 v100, 0
	v_mov_b32_e32 v99, 0
	v_mov_b32_e32 v98, 0
	v_mov_b32_e32 v75, 0
	v_mov_b32_e32 v74, 0
	v_mov_b32_e32 v77, 0
	v_mov_b32_e32 v76, 0
	v_mov_b32_e32 v79, 0
	v_mov_b32_e32 v78, 0
	v_mov_b32_e32 v81, 0
	v_mov_b32_e32 v80, 0
	v_mov_b32_e32 v151, 0
	v_mov_b32_e32 v150, 0
	v_mov_b32_e32 v153, 0
	v_mov_b32_e32 v152, 0
	v_mov_b32_e32 v155, 0
	v_mov_b32_e32 v154, 0
	v_mov_b32_e32 v157, 0
	v_mov_b32_e32 v156, 0
	v_mov_b32_e32 v119, 0
	v_mov_b32_e32 v118, 0
	v_mov_b32_e32 v121, 0
	v_mov_b32_e32 v120, 0
	v_mov_b32_e32 v123, 0
	v_mov_b32_e32 v122, 0
	v_mov_b32_e32 v125, 0
	v_mov_b32_e32 v124, 0
	v_mov_b32_e32 v103, 0
	v_mov_b32_e32 v102, 0
	v_mov_b32_e32 v105, 0
	v_mov_b32_e32 v104, 0
	v_mov_b32_e32 v107, 0
	v_mov_b32_e32 v106, 0
	v_mov_b32_e32 v109, 0
	v_mov_b32_e32 v108, 0
	v_mov_b32_e32 v87, 0
	v_mov_b32_e32 v86, 0
	v_mov_b32_e32 v89, 0
	v_mov_b32_e32 v88, 0
	v_mov_b32_e32 v91, 0
	v_mov_b32_e32 v90, 0
	v_mov_b32_e32 v93, 0
	v_mov_b32_e32 v92, 0
	v_mov_b32_e32 v65, 0
	v_mov_b32_e32 v64, 0
	v_mov_b32_e32 v63, 0
	v_mov_b32_e32 v62, 0
	v_mov_b32_e32 v67, 0
	v_mov_b32_e32 v66, 0
	v_mov_b32_e32 v69, 0
	v_mov_b32_e32 v68, 0
	v_mov_b32_e32 v47, 0
	v_mov_b32_e32 v46, 0
	v_mov_b32_e32 v49, 0
	v_mov_b32_e32 v48, 0
	v_mov_b32_e32 v53, 0
	v_mov_b32_e32 v52, 0
	v_mov_b32_e32 v51, 0
	v_mov_b32_e32 v50, 0
	v_mov_b32_e32 v23, 0
	v_mov_b32_e32 v22, 0
	v_mov_b32_e32 v25, 0
	v_mov_b32_e32 v24, 0
	v_mov_b32_e32 v31, 0
	v_mov_b32_e32 v30, 0
	v_mov_b32_e32 v33, 0
	v_mov_b32_e32 v32, 0
	v_mov_b32_e32 v11, 0
	v_mov_b32_e32 v10, 0
	v_mov_b32_e32 v13, 0
	v_mov_b32_e32 v12, 0
	v_mov_b32_e32 v15, 0
	v_mov_b32_e32 v14, 0
	v_mov_b32_e32 v17, 0
	v_mov_b32_e32 v16, 0
	v_mov_b32_e32 v71, 0
	v_mov_b32_e32 v70, 0
	v_mov_b32_e32 v73, 0
	v_mov_b32_e32 v72, 0
	v_mov_b32_e32 v83, 0
	v_mov_b32_e32 v82, 0
	v_mov_b32_e32 v85, 0
	v_mov_b32_e32 v84, 0
	v_mov_b32_e32 v55, 0
	v_mov_b32_e32 v54, 0
	v_mov_b32_e32 v57, 0
	v_mov_b32_e32 v56, 0
	v_mov_b32_e32 v59, 0
	v_mov_b32_e32 v58, 0
	v_mov_b32_e32 v61, 0
	v_mov_b32_e32 v60, 0
	v_mov_b32_e32 v35, 0
	v_mov_b32_e32 v34, 0
	v_mov_b32_e32 v37, 0
	v_mov_b32_e32 v36, 0
	v_mov_b32_e32 v39, 0
	v_mov_b32_e32 v38, 0
	v_mov_b32_e32 v41, 0
	v_mov_b32_e32 v40, 0
	v_mov_b32_e32 v9, 0
	v_mov_b32_e32 v8, 0
	v_mov_b32_e32 v7, 0
	v_mov_b32_e32 v6, 0
	v_mov_b32_e32 v5, 0
	v_mov_b32_e32 v4, 0
	v_mov_b32_e32 v3, 0
	v_mov_b32_e32 v2, 0
.Lzt_1:
	s_cbranch_vccnz .LBB0_305
	s_add_u32 s67, s30, 0x100
	v_mov_b32_e32 v2, 0
	s_addc_u32 s68, s31, 0
	s_mov_b32 s34, 0
	v_mov_b32_e32 v3, v2
	v_mov_b32_e32 v4, v2
	v_mov_b32_e32 v5, v2
	v_mov_b32_e32 v6, v2
	v_mov_b32_e32 v7, v2
	v_mov_b32_e32 v8, v2
	v_mov_b32_e32 v9, v2
	v_mov_b32_e32 v10, v2
	v_mov_b32_e32 v11, v2
	v_mov_b32_e32 v12, v2
	v_mov_b32_e32 v13, v2
	v_mov_b32_e32 v14, v2
	v_mov_b32_e32 v15, v2
	v_mov_b32_e32 v16, v2
	v_mov_b32_e32 v17, v2
	v_mov_b32_e32 v22, v2
	v_mov_b32_e32 v23, v2
	v_mov_b32_e32 v24, v2
	v_mov_b32_e32 v25, v2
	v_mov_b32_e32 v30, v2
	v_mov_b32_e32 v31, v2
	v_mov_b32_e32 v32, v2
	v_mov_b32_e32 v33, v2
	v_mov_b32_e32 v38, v2
	v_mov_b32_e32 v39, v2
	v_mov_b32_e32 v40, v2
	v_mov_b32_e32 v41, v2
	v_mov_b32_e32 v46, v2
	v_mov_b32_e32 v47, v2
	v_mov_b32_e32 v48, v2
	v_mov_b32_e32 v49, v2
	v_mov_b32_e32 v18, v2
	v_mov_b32_e32 v19, v2
	v_mov_b32_e32 v20, v2
	v_mov_b32_e32 v21, v2
	v_mov_b32_e32 v26, v2
	v_mov_b32_e32 v27, v2
	v_mov_b32_e32 v28, v2
	v_mov_b32_e32 v29, v2
	v_mov_b32_e32 v34, v2
	v_mov_b32_e32 v35, v2
	v_mov_b32_e32 v36, v2
	v_mov_b32_e32 v37, v2
	v_mov_b32_e32 v42, v2
	v_mov_b32_e32 v43, v2
	v_mov_b32_e32 v44, v2
	v_mov_b32_e32 v45, v2
	v_mov_b32_e32 v50, v2
	v_mov_b32_e32 v51, v2
	v_mov_b32_e32 v52, v2
	v_mov_b32_e32 v53, v2
	v_mov_b32_e32 v54, v2
	v_mov_b32_e32 v55, v2
	v_mov_b32_e32 v56, v2
	v_mov_b32_e32 v57, v2
	v_mov_b32_e32 v58, v2
	v_mov_b32_e32 v59, v2
	v_mov_b32_e32 v60, v2
	v_mov_b32_e32 v61, v2
	v_mov_b32_e32 v62, v2
	v_mov_b32_e32 v63, v2
	v_mov_b32_e32 v64, v2
	v_mov_b32_e32 v65, v2
	v_mov_b32_e32 v66, v2
	v_mov_b32_e32 v67, v2
	v_mov_b32_e32 v68, v2
	v_mov_b32_e32 v69, v2
	v_mov_b32_e32 v70, v2
	v_mov_b32_e32 v71, v2
	v_mov_b32_e32 v72, v2
	v_mov_b32_e32 v73, v2
	v_mov_b32_e32 v74, v2
	v_mov_b32_e32 v75, v2
	v_mov_b32_e32 v76, v2
	v_mov_b32_e32 v77, v2
	v_mov_b32_e32 v78, v2
	v_mov_b32_e32 v79, v2
	v_mov_b32_e32 v80, v2
	v_mov_b32_e32 v81, v2
	v_mov_b32_e32 v86, v2
	v_mov_b32_e32 v87, v2
	v_mov_b32_e32 v88, v2
	v_mov_b32_e32 v89, v2
	v_mov_b32_e32 v94, v2
	v_mov_b32_e32 v95, v2
	v_mov_b32_e32 v96, v2
	v_mov_b32_e32 v97, v2
	v_mov_b32_e32 v102, v2
	v_mov_b32_e32 v103, v2
	v_mov_b32_e32 v104, v2
	v_mov_b32_e32 v105, v2
	v_mov_b32_e32 v110, v2
	v_mov_b32_e32 v111, v2
	v_mov_b32_e32 v112, v2
	v_mov_b32_e32 v113, v2
	v_mov_b32_e32 v82, v2
	v_mov_b32_e32 v83, v2
	v_mov_b32_e32 v84, v2
	v_mov_b32_e32 v85, v2
	v_mov_b32_e32 v90, v2
	v_mov_b32_e32 v91, v2
	v_mov_b32_e32 v92, v2
	v_mov_b32_e32 v93, v2
	v_mov_b32_e32 v98, v2
	v_mov_b32_e32 v99, v2
	v_mov_b32_e32 v100, v2
	v_mov_b32_e32 v101, v2
	v_mov_b32_e32 v106, v2
	v_mov_b32_e32 v107, v2
	v_mov_b32_e32 v108, v2
	v_mov_b32_e32 v109, v2
	v_mov_b32_e32 v114, v2
	v_mov_b32_e32 v115, v2
	v_mov_b32_e32 v116, v2
	v_mov_b32_e32 v117, v2
	v_mov_b32_e32 v118, v2
	v_mov_b32_e32 v119, v2
	v_mov_b32_e32 v120, v2
	v_mov_b32_e32 v121, v2
	v_mov_b32_e32 v122, v2
	v_mov_b32_e32 v123, v2
	v_mov_b32_e32 v124, v2
	v_mov_b32_e32 v125, v2
	v_mov_b32_e32 v126, v2
	v_mov_b32_e32 v127, v2
	v_mov_b32_e32 v128, v2
	v_mov_b32_e32 v129, v2

;     ...
;         for (int t = 0; t < nt; t += 2) {
;     ...
; #pragma unroll
;         for (int a = 0; a < 2; ++a)
; #pragma unroll
;             for (int b = 0; b < 2; ++b)
; #pragma unroll
;                 for (int m = 0; m < 4; ++m)
; #pragma unroll
;                     for (int n = 0; n < 2; ++n) acc[a][b][m][n] = (f32x4){0.f, 0.f, 0.f, 0.f};
.LBB0_920:
	v_mov_b32_e32 v129, 0
	s_andn2_b64 vcc, exec, s[12:13]
	s_cbranch_vccz .Lzt_2
	v_mov_b32_e32 v128, 0
	v_mov_b32_e32 v127, 0
	v_mov_b32_e32 v126, 0
	v_mov_b32_e32 v125, 0
	v_mov_b32_e32 v124, 0
	v_mov_b32_e32 v123, 0
	v_mov_b32_e32 v122, 0
	v_mov_b32_e32 v121, 0
	v_mov_b32_e32 v120, 0
	v_mov_b32_e32 v119, 0
	v_mov_b32_e32 v118, 0
	v_mov_b32_e32 v117, 0
	v_mov_b32_e32 v116, 0
	v_mov_b32_e32 v115, 0
	v_mov_b32_e32 v114, 0
	v_mov_b32_e32 v95, 0
	v_mov_b32_e32 v94, 0
	v_mov_b32_e32 v97, 0
	v_mov_b32_e32 v96, 0
	v_mov_b32_e32 v101, 0
	v_mov_b32_e32 v100, 0
	v_mov_b32_e32 v99, 0
	v_mov_b32_e32 v98, 0
	v_mov_b32_e32 v75, 0
	v_mov_b32_e32 v74, 0
	v_mov_b32_e32 v87, 0
	v_mov_b32_e32 v86, 0
	v_mov_b32_e32 v85, 0
	v_mov_b32_e32 v84, 0
	v_mov_b32_e32 v89, 0
	v_mov_b32_e32 v88, 0
	v_mov_b32_e32 v153, 0
	v_mov_b32_e32 v152, 0
	v_mov_b32_e32 v155, 0
	v_mov_b32_e32 v154, 0
	v_mov_b32_e32 v157, 0
	v_mov_b32_e32 v156, 0
	v_mov_b32_e32 v159, 0
	v_mov_b32_e32 v158, 0
	v_mov_b32_e32 v161, 0
	v_mov_b32_e32 v160, 0
	v_mov_b32_e32 v147, 0
	v_mov_b32_e32 v146, 0
	v_mov_b32_e32 v151, 0
	v_mov_b32_e32 v150, 0
	v_mov_b32_e32 v149, 0
	v_mov_b32_e32 v148, 0
	v_mov_b32_e32 v107, 0
	v_mov_b32_e32 v106, 0
	v_mov_b32_e32 v109, 0
	v_mov_b32_e32 v108, 0
	v_mov_b32_e32 v111, 0
	v_mov_b32_e32 v110, 0
	v_mov_b32_e32 v113, 0
	v_mov_b32_e32 v112, 0
	v_mov_b32_e32 v91, 0
	v_mov_b32_e32 v90, 0
	v_mov_b32_e32 v93, 0
	v_mov_b32_e32 v92, 0
	v_mov_b32_e32 v103, 0
	v_mov_b32_e32 v102, 0
	v_mov_b32_e32 v105, 0
	v_mov_b32_e32 v104, 0
	v_mov_b32_e32 v73, 0
	v_mov_b32_e32 v72, 0
	v_mov_b32_e32 v71, 0
	v_mov_b32_e32 v70, 0
	v_mov_b32_e32 v83, 0
	v_mov_b32_e32 v82, 0
	v_mov_b32_e32 v81, 0
	v_mov_b32_e32 v80, 0
	v_mov_b32_e32 v57, 0
	v_mov_b32_e32 v56, 0
	v_mov_b32_e32 v55, 0
	v_mov_b32_e32 v54, 0
	v_mov_b32_e32 v65, 0
	v_mov_b32_e32 v64, 0
	v_mov_b32_e32 v63, 0
	v_mov_b32_e32 v62, 0
	v_mov_b32_e32 v41, 0
	v_mov_b32_e32 v40, 0
	v_mov_b32_e32 v39, 0
	v_mov_b32_e32 v38, 0
	v_mov_b32_e32 v49, 0
	v_mov_b32_e32 v48, 0
	v_mov_b32_e32 v47, 0
	v_mov_b32_e32 v46, 0
	v_mov_b32_e32 v25, 0
	v_mov_b32_e32 v24, 0
	v_mov_b32_e32 v23, 0
	v_mov_b32_e32 v22, 0
	v_mov_b32_e32 v33, 0
	v_mov_b32_e32 v32, 0
	v_mov_b32_e32 v31, 0
	v_mov_b32_e32 v30, 0
	v_mov_b32_e32 v69, 0
	v_mov_b32_e32 v68, 0
	v_mov_b32_e32 v67, 0
	v_mov_b32_e32 v66, 0
	v_mov_b32_e32 v79, 0
	v_mov_b32_e32 v78, 0
	v_mov_b32_e32 v77, 0
	v_mov_b32_e32 v76, 0
	v_mov_b32_e32 v53, 0
	v_mov_b32_e32 v52, 0
	v_mov_b32_e32 v51, 0
	v_mov_b32_e32 v50, 0
	v_mov_b32_e32 v61, 0
	v_mov_b32_e32 v60, 0
	v_mov_b32_e32 v59, 0
	v_mov_b32_e32 v58, 0
	v_mov_b32_e32 v37, 0
	v_mov_b32_e32 v36, 0
	v_mov_b32_e32 v35, 0
	v_mov_b32_e32 v34, 0
	v_mov_b32_e32 v45, 0
	v_mov_b32_e32 v44, 0
	v_mov_b32_e32 v43, 0
	v_mov_b32_e32 v42, 0
	v_mov_b32_e32 v21, 0
	v_mov_b32_e32 v20, 0
	v_mov_b32_e32 v19, 0
	v_mov_b32_e32 v18, 0
	v_mov_b32_e32 v29, 0
	v_mov_b32_e32 v28, 0
	v_mov_b32_e32 v27, 0
	v_mov_b32_e32 v26, 0
.Lzt_2:
	s_cbranch_vccnz .LBB0_924
	s_add_u32 s65, s28, 0x100
	v_mov_b32_e32 v2, 0
	s_addc_u32 s66, s29, 0
	s_mov_b32 s30, 0
	v_mov_b32_e32 v3, v2
	v_mov_b32_e32 v4, v2
	v_mov_b32_e32 v5, v2
	v_mov_b32_e32 v6, v2
	v_mov_b32_e32 v7, v2
	v_mov_b32_e32 v8, v2
	v_mov_b32_e32 v9, v2
	v_mov_b32_e32 v10, v2
	v_mov_b32_e32 v11, v2
	v_mov_b32_e32 v12, v2
	v_mov_b32_e32 v13, v2
	v_mov_b32_e32 v14, v2
	v_mov_b32_e32 v15, v2
	v_mov_b32_e32 v16, v2
	v_mov_b32_e32 v17, v2
	v_mov_b32_e32 v22, v2
	v_mov_b32_e32 v23, v2
	v_mov_b32_e32 v24, v2
	v_mov_b32_e32 v25, v2
	v_mov_b32_e32 v30, v2
	v_mov_b32_e32 v31, v2
	v_mov_b32_e32 v32, v2
	v_mov_b32_e32 v33, v2
	v_mov_b32_e32 v38, v2
	v_mov_b32_e32 v39, v2
	v_mov_b32_e32 v40, v2
	v_mov_b32_e32 v41, v2
	v_mov_b32_e32 v46, v2
	v_mov_b32_e32 v47, v2
	v_mov_b32_e32 v48, v2
	v_mov_b32_e32 v49, v2
	v_mov_b32_e32 v18, v2
	v_mov_b32_e32 v19, v2
	v_mov_b32_e32 v20, v2
	v_mov_b32_e32 v21, v2
	v_mov_b32_e32 v26, v2
	v_mov_b32_e32 v27, v2
	v_mov_b32_e32 v28, v2
	v_mov_b32_e32 v29, v2
	v_mov_b32_e32 v34, v2
	v_mov_b32_e32 v35, v2
	v_mov_b32_e32 v36, v2
	v_mov_b32_e32 v37, v2
	v_mov_b32_e32 v42, v2
	v_mov_b32_e32 v43, v2
	v_mov_b32_e32 v44, v2
	v_mov_b32_e32 v45, v2
	v_mov_b32_e32 v50, v2
	v_mov_b32_e32 v51, v2
	v_mov_b32_e32 v52, v2
	v_mov_b32_e32 v53, v2
	v_mov_b32_e32 v54, v2
	v_mov_b32_e32 v55, v2
	v_mov_b32_e32 v56, v2
	v_mov_b32_e32 v57, v2
	v_mov_b32_e32 v58, v2
	v_mov_b32_e32 v59, v2
	v_mov_b32_e32 v60, v2
	v_mov_b32_e32 v61, v2
	v_mov_b32_e32 v62, v2
	v_mov_b32_e32 v63, v2
	v_mov_b32_e32 v64, v2
	v_mov_b32_e32 v65, v2
	v_mov_b32_e32 v66, v2
	v_mov_b32_e32 v67, v2
	v_mov_b32_e32 v68, v2
	v_mov_b32_e32 v69, v2
	v_mov_b32_e32 v70, v2
	v_mov_b32_e32 v71, v2
	v_mov_b32_e32 v72, v2
	v_mov_b32_e32 v73, v2
	v_mov_b32_e32 v74, v2
	v_mov_b32_e32 v75, v2
	v_mov_b32_e32 v76, v2
	v_mov_b32_e32 v77, v2
	v_mov_b32_e32 v78, v2
	v_mov_b32_e32 v79, v2
	v_mov_b32_e32 v80, v2
	v_mov_b32_e32 v81, v2
	v_mov_b32_e32 v86, v2
	v_mov_b32_e32 v87, v2
	v_mov_b32_e32 v88, v2
	v_mov_b32_e32 v89, v2
	v_mov_b32_e32 v94, v2
	v_mov_b32_e32 v95, v2
	v_mov_b32_e32 v96, v2
	v_mov_b32_e32 v97, v2
	v_mov_b32_e32 v102, v2
	v_mov_b32_e32 v103, v2
	v_mov_b32_e32 v104, v2
	v_mov_b32_e32 v105, v2
	v_mov_b32_e32 v110, v2
	v_mov_b32_e32 v111, v2
	v_mov_b32_e32 v112, v2
	v_mov_b32_e32 v113, v2
	v_mov_b32_e32 v82, v2
	v_mov_b32_e32 v83, v2
	v_mov_b32_e32 v84, v2
	v_mov_b32_e32 v85, v2
	v_mov_b32_e32 v90, v2
	v_mov_b32_e32 v91, v2
	v_mov_b32_e32 v92, v2
	v_mov_b32_e32 v93, v2
	v_mov_b32_e32 v98, v2
	v_mov_b32_e32 v99, v2
	v_mov_b32_e32 v100, v2
	v_mov_b32_e32 v101, v2
	v_mov_b32_e32 v106, v2
	v_mov_b32_e32 v107, v2
	v_mov_b32_e32 v108, v2
	v_mov_b32_e32 v109, v2
	v_mov_b32_e32 v114, v2
	v_mov_b32_e32 v115, v2
	v_mov_b32_e32 v116, v2
	v_mov_b32_e32 v117, v2
	v_mov_b32_e32 v118, v2
	v_mov_b32_e32 v119, v2
	v_mov_b32_e32 v120, v2
	v_mov_b32_e32 v121, v2
	v_mov_b32_e32 v122, v2
	v_mov_b32_e32 v123, v2
	v_mov_b32_e32 v124, v2
	v_mov_b32_e32 v125, v2
	v_mov_b32_e32 v126, v2
	v_mov_b32_e32 v127, v2
	v_mov_b32_e32 v128, v2
	v_mov_b32_e32 v129, v2

;     ...
;         for (int t = 0; t < nt; t += 2) {
;     ...
; #pragma unroll
;         for (int a = 0; a < 2; ++a)
; #pragma unroll
;             for (int b = 0; b < 2; ++b)
; #pragma unroll
;                 for (int m = 0; m < 4; ++m)
; #pragma unroll
;                     for (int n = 0; n < 2; ++n) acc[a][b][m][n] = (f32x4){0.f, 0.f, 0.f, 0.f};
.LBB0_1410:
	s_ashr_i32 s17, s16, 31
	s_lshl_b64 s[18:19], s[16:17], 19
	s_add_u32 s18, s37, s18
	s_addc_u32 s19, s38, s19
	s_ashr_i32 s15, s14, 31
	s_lshl_b64 s[20:21], s[14:15], 19
	s_add_u32 s20, s39, s20
	s_addc_u32 s21, s40, s21
	v_mov_b32_e32 v127, 0
	s_andn2_b64 vcc, exec, s[10:11]
	s_cbranch_vccz .Lzt_4
	v_mov_b32_e32 v126, 0
	v_mov_b32_e32 v151, 0
	v_mov_b32_e32 v150, 0
	v_mov_b32_e32 v125, 0
	v_mov_b32_e32 v124, 0
	v_mov_b32_e32 v123, 0
	v_mov_b32_e32 v122, 0
	v_mov_b32_e32 v155, 0
	v_mov_b32_e32 v154, 0
	v_mov_b32_e32 v153, 0
	v_mov_b32_e32 v152, 0
	v_mov_b32_e32 v157, 0
	v_mov_b32_e32 v156, 0
	v_mov_b32_e32 v129, 0
	v_mov_b32_e32 v128, 0
	v_mov_b32_e32 v105, 0
	v_mov_b32_e32 v104, 0
	v_mov_b32_e32 v103, 0
	v_mov_b32_e32 v102, 0
	v_mov_b32_e32 v101, 0
	v_mov_b32_e32 v100, 0
	v_mov_b32_e32 v99, 0
	v_mov_b32_e32 v98, 0
	v_mov_b32_e32 v81, 0
	v_mov_b32_e32 v80, 0
	v_mov_b32_e32 v77, 0
	v_mov_b32_e32 v76, 0
	v_mov_b32_e32 v79, 0
	v_mov_b32_e32 v78, 0
	v_mov_b32_e32 v75, 0
	v_mov_b32_e32 v74, 0
	v_mov_b32_e32 v161, 0
	v_mov_b32_e32 v160, 0
	v_mov_b32_e32 v159, 0
	v_mov_b32_e32 v158, 0
	v_mov_b32_e32 v165, 0
	v_mov_b32_e32 v164, 0
	v_mov_b32_e32 v163, 0
	v_mov_b32_e32 v162, 0
	v_mov_b32_e32 v121, 0
	v_mov_b32_e32 v120, 0
	v_mov_b32_e32 v117, 0
	v_mov_b32_e32 v116, 0
	v_mov_b32_e32 v119, 0
	v_mov_b32_e32 v118, 0
	v_mov_b32_e32 v115, 0
	v_mov_b32_e32 v114, 0
	v_mov_b32_e32 v113, 0
	v_mov_b32_e32 v112, 0
	v_mov_b32_e32 v109, 0
	v_mov_b32_e32 v108, 0
	v_mov_b32_e32 v111, 0
	v_mov_b32_e32 v110, 0
	v_mov_b32_e32 v107, 0
	v_mov_b32_e32 v106, 0
	v_mov_b32_e32 v97, 0
	v_mov_b32_e32 v96, 0
	v_mov_b32_e32 v93, 0
	v_mov_b32_e32 v92, 0
	v_mov_b32_e32 v95, 0
	v_mov_b32_e32 v94, 0
	v_mov_b32_e32 v91, 0
	v_mov_b32_e32 v90, 0
	v_mov_b32_e32 v73, 0
	v_mov_b32_e32 v72, 0
	v_mov_b32_e32 v69, 0
	v_mov_b32_e32 v68, 0
	v_mov_b32_e32 v71, 0
	v_mov_b32_e32 v70, 0
	v_mov_b32_e32 v67, 0
	v_mov_b32_e32 v66, 0
	v_mov_b32_e32 v57, 0
	v_mov_b32_e32 v56, 0
	v_mov_b32_e32 v55, 0
	v_mov_b32_e32 v54, 0
	v_mov_b32_e32 v53, 0
	v_mov_b32_e32 v52, 0
	v_mov_b32_e32 v51, 0
	v_mov_b32_e32 v50, 0
	v_mov_b32_e32 v41, 0
	v_mov_b32_e32 v40, 0
	v_mov_b32_e32 v39, 0
	v_mov_b32_e32 v38, 0
	v_mov_b32_e32 v37, 0
	v_mov_b32_e32 v36, 0
	v_mov_b32_e32 v35, 0
	v_mov_b32_e32 v34, 0
	v_mov_b32_e32 v25, 0
	v_mov_b32_e32 v24, 0
	v_mov_b32_e32 v23, 0
	v_mov_b32_e32 v22, 0
	v_mov_b32_e32 v21, 0
	v_mov_b32_e32 v20, 0
	v_mov_b32_e32 v19, 0
	v_mov_b32_e32 v18, 0
	v_mov_b32_e32 v89, 0
	v_mov_b32_e32 v88, 0
	v_mov_b32_e32 v85, 0
	v_mov_b32_e32 v84, 0
	v_mov_b32_e32 v87, 0
	v_mov_b32_e32 v86, 0
	v_mov_b32_e32 v83, 0
	v_mov_b32_e32 v82, 0
	v_mov_b32_e32 v65, 0
	v_mov_b32_e32 v64, 0
	v_mov_b32_e32 v61, 0
	v_mov_b32_e32 v60, 0
	v_mov_b32_e32 v63, 0
	v_mov_b32_e32 v62, 0
	v_mov_b32_e32 v59, 0
	v_mov_b32_e32 v58, 0
	v_mov_b32_e32 v49, 0
	v_mov_b32_e32 v48, 0
	v_mov_b32_e32 v45, 0
	v_mov_b32_e32 v44, 0
	v_mov_b32_e32 v47, 0
	v_mov_b32_e32 v46, 0
	v_mov_b32_e32 v43, 0
	v_mov_b32_e32 v42, 0
	v_mov_b32_e32 v33, 0
	v_mov_b32_e32 v32, 0
	v_mov_b32_e32 v29, 0
	v_mov_b32_e32 v28, 0
	v_mov_b32_e32 v31, 0
	v_mov_b32_e32 v30, 0
	v_mov_b32_e32 v27, 0
	v_mov_b32_e32 v26, 0
.Lzt_4:
	s_cbranch_vccnz .LBB0_1414
	s_and_b64 s[28:29], s[0:1], exec
	s_cselect_b32 s15, s19, s27
	s_cselect_b32 s17, s18, s26
	s_cselect_b32 s64, s21, s25
	s_cselect_b32 s65, s20, s24
	s_add_u32 s66, s24, 0x100
	s_addc_u32 s67, s25, 0
	s_add_u32 s24, s26, 0x40080
	s_addc_u32 s25, s27, 0
	s_mov_b32 s26, 0
	v_mov_b32_e32 v2, 0
	v_mov_b32_e32 v3, 0
	v_mov_b32_e32 v4, 0
	v_mov_b32_e32 v5, 0
	v_mov_b32_e32 v6, 0
	v_mov_b32_e32 v7, 0
	v_mov_b32_e32 v8, 0
	v_mov_b32_e32 v9, 0
	v_mov_b32_e32 v10, 0
	v_mov_b32_e32 v11, 0
	v_mov_b32_e32 v12, 0
	v_mov_b32_e32 v13, 0
	v_mov_b32_e32 v14, 0
	v_mov_b32_e32 v15, 0
	v_mov_b32_e32 v16, 0
	v_mov_b32_e32 v17, 0
	v_mov_b32_e32 v22, 0
	v_mov_b32_e32 v23, 0
	v_mov_b32_e32 v24, 0
	v_mov_b32_e32 v25, 0
	v_mov_b32_e32 v30, 0
	v_mov_b32_e32 v31, 0
	v_mov_b32_e32 v32, 0
	v_mov_b32_e32 v33, 0
	v_mov_b32_e32 v38, 0
	v_mov_b32_e32 v39, 0
	v_mov_b32_e32 v40, 0
	v_mov_b32_e32 v41, 0
	v_mov_b32_e32 v46, 0
	v_mov_b32_e32 v47, 0
	v_mov_b32_e32 v48, 0
	v_mov_b32_e32 v49, 0
	v_mov_b32_e32 v18, 0
	v_mov_b32_e32 v19, 0
	v_mov_b32_e32 v20, 0
	v_mov_b32_e32 v21, 0
	v_mov_b32_e32 v26, 0
	v_mov_b32_e32 v27, 0
	v_mov_b32_e32 v28, 0
	v_mov_b32_e32 v29, 0
	v_mov_b32_e32 v34, 0
	v_mov_b32_e32 v35, 0
	v_mov_b32_e32 v36, 0
	v_mov_b32_e32 v37, 0
	v_mov_b32_e32 v42, 0
	v_mov_b32_e32 v43, 0
	v_mov_b32_e32 v44, 0
	v_mov_b32_e32 v45, 0
	v_mov_b32_e32 v50, 0
	v_mov_b32_e32 v51, 0
	v_mov_b32_e32 v52, 0
	v_mov_b32_e32 v53, 0
	v_mov_b32_e32 v54, 0
	v_mov_b32_e32 v55, 0
	v_mov_b32_e32 v56, 0
	v_mov_b32_e32 v57, 0
	v_mov_b32_e32 v58, 0
	v_mov_b32_e32 v59, 0
	v_mov_b32_e32 v60, 0
	v_mov_b32_e32 v61, 0
	v_mov_b32_e32 v62, 0
	v_mov_b32_e32 v63, 0
	v_mov_b32_e32 v64, 0
	v_mov_b32_e32 v65, 0
	v_mov_b32_e32 v66, 0
	v_mov_b32_e32 v67, 0
	v_mov_b32_e32 v68, 0
	v_mov_b32_e32 v69, 0
	v_mov_b32_e32 v70, 0
	v_mov_b32_e32 v71, 0
	v_mov_b32_e32 v72, 0
	v_mov_b32_e32 v73, 0
	v_mov_b32_e32 v74, 0
	v_mov_b32_e32 v75, 0
	v_mov_b32_e32 v76, 0
	v_mov_b32_e32 v77, 0
	v_mov_b32_e32 v78, 0
	v_mov_b32_e32 v79, 0
	v_mov_b32_e32 v80, 0
	v_mov_b32_e32 v81, 0
	v_mov_b32_e32 v86, 0
	v_mov_b32_e32 v87, 0
	v_mov_b32_e32 v88, 0
	v_mov_b32_e32 v89, 0
	v_mov_b32_e32 v94, 0
	v_mov_b32_e32 v95, 0
	v_mov_b32_e32 v96, 0
	v_mov_b32_e32 v97, 0
	v_mov_b32_e32 v102, 0
	v_mov_b32_e32 v103, 0
	v_mov_b32_e32 v104, 0
	v_mov_b32_e32 v105, 0
	v_mov_b32_e32 v110, 0
	v_mov_b32_e32 v111, 0
	v_mov_b32_e32 v112, 0
	v_mov_b32_e32 v113, 0
	v_mov_b32_e32 v82, 0
	v_mov_b32_e32 v83, 0
	v_mov_b32_e32 v84, 0
	v_mov_b32_e32 v85, 0
	v_mov_b32_e32 v90, 0
	v_mov_b32_e32 v91, 0
	v_mov_b32_e32 v92, 0
	v_mov_b32_e32 v93, 0
	v_mov_b32_e32 v98, 0
	v_mov_b32_e32 v99, 0
	v_mov_b32_e32 v100, 0
	v_mov_b32_e32 v101, 0
	v_mov_b32_e32 v106, 0
	v_mov_b32_e32 v107, 0
	v_mov_b32_e32 v108, 0
	v_mov_b32_e32 v109, 0
	v_mov_b32_e32 v114, 0
	v_mov_b32_e32 v115, 0
	v_mov_b32_e32 v116, 0
	v_mov_b32_e32 v117, 0
	v_mov_b32_e32 v118, 0
	v_mov_b32_e32 v119, 0
	v_mov_b32_e32 v120, 0
	v_mov_b32_e32 v121, 0
	v_mov_b32_e32 v122, 0
	v_mov_b32_e32 v123, 0
	v_mov_b32_e32 v124, 0
	v_mov_b32_e32 v125, 0
	v_mov_b32_e32 v126, 0
	v_mov_b32_e32 v127, 0
	v_mov_b32_e32 v128, 0
	v_mov_b32_e32 v129, 0
